# K2 iso_g stores merged into tile epilogue (separate loop removed)
# speedup vs baseline: 1.0632x; 1.0033x over previous
.LBB1_162:
.LBB1_167:
	s_or_b64 exec, exec, s[0:1]
	v_mov_b32_e32 v41, 0x18500
	v_or_b32_e32 v36, v165, v166
	v_or_b32_e32 v37, v158, v166
	v_or_b32_e32 v38, v150, v166
	v_or_b32_e32 v39, v146, v166
	v_lshl_or_b32 v40, v164, 4, v166
	v_add_u32_e32 v40, 0x140, v40
	v_lshl_add_u32 v36, v36, 2, v41
	v_lshl_add_u32 v37, v37, 2, v41
	v_lshl_add_u32 v38, v38, 2, v41
	v_lshl_add_u32 v39, v39, 2, v41
	v_lshl_add_u32 v40, v40, 2, v41
	ds_read_b32 v36, v36
	ds_read_b32 v37, v37
	ds_read_b32 v38, v38
	ds_read_b32 v39, v39
	ds_read_b32 v40, v40
	v_or_b32_e32 v23, v165, v166
	v_lshlrev_b32_e32 v0, 3, v167
	v_mov_b32_e32 v1, 0
	v_add_u32_e32 v22, s30, v23
	s_mov_b32 s2, 0x186a0
	v_lshl_add_u64 v[0:1], s[28:29], 0, v[0:1]
	v_cmp_gt_i32_e32 vcc, s2, v22
	s_and_saveexec_b64 s[0:1], vcc
	s_cbranch_execz .LBB1_169
	v_mov_b32_e32 v24, 0x18500
	v_lshl_add_u32 v23, v23, 2, v24
	s_waitcnt lgkmcnt(0)
	v_mov_b32_e32 v23, v36
	v_cvt_f32_u32_e32 v23, v23
	v_max_f32_e32 v23, 1.0, v23
	v_rsq_f32_e32 v24, v23
	v_lshlrev_b32_e32 v42, 2, v22
	s_mov_b64 s[6:7], exec
	v_cmp_eq_u32_e32 vcc, 0, v167
	s_and_b64 exec, exec, vcc
	global_store_dword v42, v24, s[24:25]
	s_mov_b64 exec, s[6:7]
	v_ashrrev_i32_e32 v23, 31, v22
	v_lshlrev_b64 v[22:23], 5, v[22:23]
	v_pk_mul_f32 v[2:3], v[2:3], v[24:25] op_sel_hi:[1,0]
	v_pk_mul_f32 v[4:5], v[4:5], v[24:25] op_sel_hi:[1,0]
	v_cvt_pk_bf16_f32 v2, v2, v3
	v_cvt_pk_bf16_f32 v3, v4, v5
	v_lshl_add_u64 v[4:5], v[0:1], 0, v[22:23]
	global_store_dwordx2 v[4:5], v[2:3], off
.LBB1_169:
	s_or_b64 exec, exec, s[0:1]
	v_or_b32_e32 v3, v158, v166
	v_add_u32_e32 v2, s30, v3
	v_cmp_gt_i32_e32 vcc, s2, v2
	s_and_saveexec_b64 s[0:1], vcc
	s_cbranch_execz .LBB1_171
	v_mov_b32_e32 v4, 0x18500
	v_lshl_add_u32 v3, v3, 2, v4
	s_waitcnt lgkmcnt(0)
	v_mov_b32_e32 v3, v37
	v_cvt_f32_u32_e32 v3, v3
	v_max_f32_e32 v3, 1.0, v3
	v_rsq_f32_e32 v4, v3
	v_lshlrev_b32_e32 v42, 2, v2
	s_mov_b64 s[6:7], exec
	v_cmp_eq_u32_e32 vcc, 0, v167
	s_and_b64 exec, exec, vcc
	global_store_dword v42, v4, s[24:25]
	s_mov_b64 exec, s[6:7]
	v_ashrrev_i32_e32 v3, 31, v2
	v_lshlrev_b64 v[2:3], 5, v[2:3]
	v_lshl_add_u64 v[2:3], v[0:1], 0, v[2:3]
	v_pk_mul_f32 v[6:7], v[6:7], v[4:5] op_sel_hi:[1,0]
	v_pk_mul_f32 v[4:5], v[8:9], v[4:5] op_sel_hi:[1,0]
	v_cvt_pk_bf16_f32 v6, v6, v7
	v_cvt_pk_bf16_f32 v7, v4, v5
	global_store_dwordx2 v[2:3], v[6:7], off
.LBB1_171:
	s_or_b64 exec, exec, s[0:1]
	v_or_b32_e32 v3, v150, v166
	v_add_u32_e32 v2, s30, v3
	v_cmp_gt_i32_e32 vcc, s2, v2
	s_and_saveexec_b64 s[0:1], vcc
	s_cbranch_execz .LBB1_173
	v_mov_b32_e32 v4, 0x18500
	v_lshl_add_u32 v3, v3, 2, v4
	s_waitcnt lgkmcnt(0)
	v_mov_b32_e32 v3, v38
	v_cvt_f32_u32_e32 v3, v3
	v_max_f32_e32 v3, 1.0, v3
	v_rsq_f32_e32 v4, v3
	v_lshlrev_b32_e32 v42, 2, v2
	s_mov_b64 s[6:7], exec
	v_cmp_eq_u32_e32 vcc, 0, v167
	s_and_b64 exec, exec, vcc
	global_store_dword v42, v4, s[24:25]
	s_mov_b64 exec, s[6:7]
	v_ashrrev_i32_e32 v3, 31, v2
	v_lshlrev_b64 v[2:3], 5, v[2:3]
	v_lshl_add_u64 v[2:3], v[0:1], 0, v[2:3]
	v_pk_mul_f32 v[6:7], v[10:11], v[4:5] op_sel_hi:[1,0]
	v_pk_mul_f32 v[4:5], v[12:13], v[4:5] op_sel_hi:[1,0]
	v_cvt_pk_bf16_f32 v6, v6, v7
	v_cvt_pk_bf16_f32 v7, v4, v5
	global_store_dwordx2 v[2:3], v[6:7], off
.LBB1_173:
	s_or_b64 exec, exec, s[0:1]
	v_or_b32_e32 v3, v146, v166
	v_add_u32_e32 v2, s30, v3
	v_cmp_gt_i32_e32 vcc, s2, v2
	s_and_saveexec_b64 s[0:1], vcc
	s_cbranch_execz .LBB1_175
	v_mov_b32_e32 v4, 0x18500
	v_lshl_add_u32 v3, v3, 2, v4
	s_waitcnt lgkmcnt(0)
	v_mov_b32_e32 v3, v39
	v_cvt_f32_u32_e32 v3, v3
	v_max_f32_e32 v3, 1.0, v3
	v_rsq_f32_e32 v4, v3
	v_lshlrev_b32_e32 v42, 2, v2
	s_mov_b64 s[6:7], exec
	v_cmp_eq_u32_e32 vcc, 0, v167
	s_and_b64 exec, exec, vcc
	global_store_dword v42, v4, s[24:25]
	s_mov_b64 exec, s[6:7]
	v_ashrrev_i32_e32 v3, 31, v2
	v_lshlrev_b64 v[2:3], 5, v[2:3]
	v_lshl_add_u64 v[2:3], v[0:1], 0, v[2:3]
	v_pk_mul_f32 v[6:7], v[14:15], v[4:5] op_sel_hi:[1,0]
	v_pk_mul_f32 v[4:5], v[16:17], v[4:5] op_sel_hi:[1,0]
	v_cvt_pk_bf16_f32 v6, v6, v7
	v_cvt_pk_bf16_f32 v7, v4, v5
	global_store_dwordx2 v[2:3], v[6:7], off
.LBB1_175:
	s_or_b64 exec, exec, s[0:1]
	v_lshl_or_b32 v2, v164, 4, v166
	v_add_u32_e32 v3, 0x140, v2
	v_add_u32_e32 v2, s30, v3
	s_mov_b32 s0, 0x186a0
	v_cmp_gt_i32_e32 vcc, s0, v2
	s_and_saveexec_b64 s[0:1], vcc
	s_cbranch_execz .LBB1_177
	v_mov_b32_e32 v4, 0x18500
	v_lshl_add_u32 v3, v3, 2, v4
	s_waitcnt lgkmcnt(0)
	v_mov_b32_e32 v3, v40
	v_cvt_f32_u32_e32 v3, v3
	v_max_f32_e32 v3, 1.0, v3
	v_rsq_f32_e32 v4, v3
	v_lshlrev_b32_e32 v42, 2, v2
	s_mov_b64 s[6:7], exec
	v_cmp_eq_u32_e32 vcc, 0, v167
	s_and_b64 exec, exec, vcc
	global_store_dword v42, v4, s[24:25]
	s_mov_b64 exec, s[6:7]
	v_ashrrev_i32_e32 v3, 31, v2
	v_lshlrev_b64 v[2:3], 5, v[2:3]
	v_lshl_add_u64 v[0:1], v[0:1], 0, v[2:3]
	v_pk_mul_f32 v[6:7], v[18:19], v[4:5] op_sel_hi:[1,0]
	v_pk_mul_f32 v[4:5], v[20:21], v[4:5] op_sel_hi:[1,0]
	v_cvt_pk_bf16_f32 v6, v6, v7
	v_cvt_pk_bf16_f32 v7, v4, v5
	global_store_dwordx2 v[0:1], v[6:7], off
